# latency ladders removed by hand in three memory-bound tails: gla_pass2 scan, router-task norm rows (P8), final combine+norm rows (P11): loads of a row issued together, per-batch column vectors kept in
# speedup vs baseline: 1.0296x; 1.0296x over previous
.LBB0_1283:
	s_or_b64 exec, exec, s[4:5]
	s_add_i32 s88, s88, s89
	v_add_u32_e32 v90, s89, v90
	s_mulk_i32 s0, 0x3000
	s_ashr_i32 s1, s0, 31
	s_lshl_b64 s[0:1], s[0:1], 2
	s_add_u32 s4, s33, s0
	s_addc_u32 s5, s84, s1
	s_add_u32 s0, s4, 0x6000
	s_addc_u32 s1, s5, 0
	s_add_u32 s10, s4, 0x8000
	s_addc_u32 s11, s5, 0
	s_add_i32 s4, s95, s85
	s_mov_b32 s12, 0x1000
	s_mov_b32 s13, 0
	v_xor_b32_e32 v184, 1, v113
	v_lshlrev_b32_e32 v184, 2, v184
	v_xor_b32_e32 v185, 2, v113
	v_lshlrev_b32_e32 v185, 2, v185
	v_xor_b32_e32 v186, 4, v113
	v_lshlrev_b32_e32 v186, 2, v186
	v_xor_b32_e32 v187, 8, v113
	v_lshlrev_b32_e32 v187, 2, v187
	v_xor_b32_e32 v188, 16, v113
	v_lshlrev_b32_e32 v188, 2, v188
	v_xor_b32_e32 v189, 32, v113
	v_lshlrev_b32_e32 v189, 2, v189
	s_ashr_i32 s5, s4, 31
	s_lshl_b64 s[8:9], s[4:5], 13
	s_lshl_b64 s[14:15], s[4:5], 11
	v_lshl_add_u64 v[178:179], v[68:69], 0, s[8:9]
	v_lshl_add_u64 v[180:181], v[178:179], 0, s[12:13]
	v_lshl_add_u64 v[182:183], v[84:85], 0, s[14:15]
	global_load_dwordx4 v[2:5], v[178:179], off offset:0
	global_load_dwordx4 v[6:9], v[178:179], off offset:1024
	global_load_dwordx4 v[10:13], v[178:179], off offset:2048
	global_load_dwordx4 v[14:17], v[178:179], off offset:3072
	global_load_dwordx4 v[18:21], v[180:181], off offset:0
	global_load_dwordx4 v[22:25], v[180:181], off offset:1024
	global_load_dwordx4 v[26:29], v[180:181], off offset:2048
	global_load_dwordx4 v[30:33], v[180:181], off offset:3072
	global_load_dwordx4 v[114:117], v[74:75], off
	global_load_dwordx4 v[118:121], v[74:75], off offset:1024
	global_load_dwordx4 v[122:125], v[74:75], off offset:2048
	global_load_dwordx4 v[126:129], v[74:75], off offset:3072
	global_load_dwordx4 v[130:133], v[76:77], off
	global_load_dwordx4 v[134:137], v[78:79], off
	global_load_dwordx4 v[138:141], v[80:81], off
	global_load_dwordx4 v[142:145], v[82:83], off
	global_load_dwordx4 v[146:149], v104, s[10:11]
	global_load_dwordx4 v[150:153], v105, s[10:11]
	global_load_dwordx4 v[154:157], v106, s[10:11]
	global_load_dwordx4 v[158:161], v107, s[10:11]
	global_load_dwordx4 v[162:165], v108, s[10:11]
	global_load_dwordx4 v[166:169], v109, s[10:11]
	global_load_dwordx4 v[170:173], v110, s[10:11]
	global_load_dwordx4 v[174:177], v111, s[10:11]
	global_load_dwordx4 v[34:37], v104, s[0:1]
	global_load_dwordx4 v[38:41], v105, s[0:1]
	global_load_dwordx4 v[42:45], v106, s[0:1]
	global_load_dwordx4 v[46:49], v107, s[0:1]
	global_load_dwordx4 v[50:53], v108, s[0:1]
	global_load_dwordx4 v[54:57], v109, s[0:1]
	global_load_dwordx4 v[58:61], v110, s[0:1]
	global_load_dwordx4 v[62:65], v111, s[0:1]
	s_waitcnt vmcnt(24)
	v_mov_b32_e32 v190, 0
	v_mul_f32_e32 v191, v2, v2
	v_fmac_f32_e32 v191, v3, v3
	v_mul_f32_e32 v192, v4, v4
	v_fmac_f32_e32 v192, v5, v5
	v_add_f32_e32 v191, v191, v192
	v_add_f32_e32 v190, v190, v191
	v_mul_f32_e32 v191, v6, v6
	v_fmac_f32_e32 v191, v7, v7
	v_mul_f32_e32 v192, v8, v8
	v_fmac_f32_e32 v192, v9, v9
	v_add_f32_e32 v191, v191, v192
	v_add_f32_e32 v190, v190, v191
	v_mul_f32_e32 v191, v10, v10
	v_fmac_f32_e32 v191, v11, v11
	v_mul_f32_e32 v192, v12, v12
	v_fmac_f32_e32 v192, v13, v13
	v_add_f32_e32 v191, v191, v192
	v_add_f32_e32 v190, v190, v191
	v_mul_f32_e32 v191, v14, v14
	v_fmac_f32_e32 v191, v15, v15
	v_mul_f32_e32 v192, v16, v16
	v_fmac_f32_e32 v192, v17, v17
	v_add_f32_e32 v191, v191, v192
	v_add_f32_e32 v190, v190, v191
	v_mul_f32_e32 v191, v18, v18
	v_fmac_f32_e32 v191, v19, v19
	v_mul_f32_e32 v192, v20, v20
	v_fmac_f32_e32 v192, v21, v21
	v_add_f32_e32 v191, v191, v192
	v_add_f32_e32 v190, v190, v191
	v_mul_f32_e32 v191, v22, v22
	v_fmac_f32_e32 v191, v23, v23
	v_mul_f32_e32 v192, v24, v24
	v_fmac_f32_e32 v192, v25, v25
	v_add_f32_e32 v191, v191, v192
	v_add_f32_e32 v190, v190, v191
	v_mul_f32_e32 v191, v26, v26
	v_fmac_f32_e32 v191, v27, v27
	v_mul_f32_e32 v192, v28, v28
	v_fmac_f32_e32 v192, v29, v29
	v_add_f32_e32 v191, v191, v192
	v_add_f32_e32 v190, v190, v191
	v_mul_f32_e32 v191, v30, v30
	v_fmac_f32_e32 v191, v31, v31
	v_mul_f32_e32 v192, v32, v32
	v_fmac_f32_e32 v192, v33, v33
	v_add_f32_e32 v191, v191, v192
	v_add_f32_e32 v190, v190, v191
	ds_bpermute_b32 v191, v184, v190
	s_waitcnt lgkmcnt(0)
	v_add_f32_e32 v190, v190, v191
	ds_bpermute_b32 v191, v185, v190
	s_waitcnt lgkmcnt(0)
	v_add_f32_e32 v190, v190, v191
	ds_bpermute_b32 v191, v186, v190
	s_waitcnt lgkmcnt(0)
	v_add_f32_e32 v190, v190, v191
	ds_bpermute_b32 v191, v187, v190
	s_waitcnt lgkmcnt(0)
	v_add_f32_e32 v190, v190, v191
	ds_bpermute_b32 v191, v188, v190
	s_waitcnt lgkmcnt(0)
	v_add_f32_e32 v190, v190, v191
	ds_bpermute_b32 v191, v189, v190
	s_waitcnt lgkmcnt(0)
	v_add_f32_e32 v190, v190, v191
	v_fmamk_f32 v66, v190, 0x3a000000, v100
	v_rsq_f32_e32 v66, v66
	s_waitcnt vmcnt(0)
	v_pk_add_f32 v[146:147], v[146:147], 1.0 op_sel_hi:[1,0]
	v_pk_add_f32 v[148:149], v[148:149], 1.0 op_sel_hi:[1,0]
	v_pk_add_f32 v[150:151], v[150:151], 1.0 op_sel_hi:[1,0]
	v_pk_add_f32 v[152:153], v[152:153], 1.0 op_sel_hi:[1,0]
	v_pk_add_f32 v[154:155], v[154:155], 1.0 op_sel_hi:[1,0]
	v_pk_add_f32 v[156:157], v[156:157], 1.0 op_sel_hi:[1,0]
	v_pk_add_f32 v[158:159], v[158:159], 1.0 op_sel_hi:[1,0]
	v_pk_add_f32 v[160:161], v[160:161], 1.0 op_sel_hi:[1,0]
	v_pk_add_f32 v[162:163], v[162:163], 1.0 op_sel_hi:[1,0]
	v_pk_add_f32 v[164:165], v[164:165], 1.0 op_sel_hi:[1,0]
	v_pk_add_f32 v[166:167], v[166:167], 1.0 op_sel_hi:[1,0]
	v_pk_add_f32 v[168:169], v[168:169], 1.0 op_sel_hi:[1,0]
	v_pk_add_f32 v[170:171], v[170:171], 1.0 op_sel_hi:[1,0]
	v_pk_add_f32 v[172:173], v[172:173], 1.0 op_sel_hi:[1,0]
	v_pk_add_f32 v[174:175], v[174:175], 1.0 op_sel_hi:[1,0]
	v_pk_add_f32 v[176:177], v[176:177], 1.0 op_sel_hi:[1,0]
	v_mul_f32_e32 v2, v2, v66
	v_mul_f32_e32 v2, v2, v114
	v_fma_f32 v2, v2, v146, v34
	v_mul_f32_e32 v2, 4.0, v2
	v_mul_f32_e32 v3, v3, v66
	v_mul_f32_e32 v3, v3, v115
	v_fma_f32 v3, v3, v147, v35
	v_mul_f32_e32 v3, 4.0, v3
	v_mul_f32_e32 v4, v4, v66
	v_mul_f32_e32 v4, v4, v116
	v_fma_f32 v4, v4, v148, v36
	v_mul_f32_e32 v4, 4.0, v4
	v_mul_f32_e32 v5, v5, v66
	v_mul_f32_e32 v5, v5, v117
	v_fma_f32 v5, v5, v149, v37
	v_mul_f32_e32 v5, 4.0, v5
	v_cvt_pk_fp8_f32 v91, v2, v3
	s_nop 0
	v_cvt_pk_fp8_f32 v91, v4, v5 op_sel:[0,0,1]
	global_store_dword v[182:183], v91, off offset:0
	v_mul_f32_e32 v6, v6, v66
	v_mul_f32_e32 v6, v6, v118
	v_fma_f32 v6, v6, v150, v38
	v_mul_f32_e32 v6, 4.0, v6
	v_mul_f32_e32 v7, v7, v66
	v_mul_f32_e32 v7, v7, v119
	v_fma_f32 v7, v7, v151, v39
	v_mul_f32_e32 v7, 4.0, v7
	v_mul_f32_e32 v8, v8, v66
	v_mul_f32_e32 v8, v8, v120
	v_fma_f32 v8, v8, v152, v40
	v_mul_f32_e32 v8, 4.0, v8
	v_mul_f32_e32 v9, v9, v66
	v_mul_f32_e32 v9, v9, v121
	v_fma_f32 v9, v9, v153, v41
	v_mul_f32_e32 v9, 4.0, v9
	v_cvt_pk_fp8_f32 v92, v6, v7
	s_nop 0
	v_cvt_pk_fp8_f32 v92, v8, v9 op_sel:[0,0,1]
	global_store_dword v[182:183], v92, off offset:256
	v_mul_f32_e32 v10, v10, v66
	v_mul_f32_e32 v10, v10, v122
	v_fma_f32 v10, v10, v154, v42
	v_mul_f32_e32 v10, 4.0, v10
	v_mul_f32_e32 v11, v11, v66
	v_mul_f32_e32 v11, v11, v123
	v_fma_f32 v11, v11, v155, v43
	v_mul_f32_e32 v11, 4.0, v11
	v_mul_f32_e32 v12, v12, v66
	v_mul_f32_e32 v12, v12, v124
	v_fma_f32 v12, v12, v156, v44
	v_mul_f32_e32 v12, 4.0, v12
	v_mul_f32_e32 v13, v13, v66
	v_mul_f32_e32 v13, v13, v125
	v_fma_f32 v13, v13, v157, v45
	v_mul_f32_e32 v13, 4.0, v13
	v_cvt_pk_fp8_f32 v93, v10, v11
	s_nop 0
	v_cvt_pk_fp8_f32 v93, v12, v13 op_sel:[0,0,1]
	global_store_dword v[182:183], v93, off offset:512
	v_mul_f32_e32 v14, v14, v66
	v_mul_f32_e32 v14, v14, v126
	v_fma_f32 v14, v14, v158, v46
	v_mul_f32_e32 v14, 4.0, v14
	v_mul_f32_e32 v15, v15, v66
	v_mul_f32_e32 v15, v15, v127
	v_fma_f32 v15, v15, v159, v47
	v_mul_f32_e32 v15, 4.0, v15
	v_mul_f32_e32 v16, v16, v66
	v_mul_f32_e32 v16, v16, v128
	v_fma_f32 v16, v16, v160, v48
	v_mul_f32_e32 v16, 4.0, v16
	v_mul_f32_e32 v17, v17, v66
	v_mul_f32_e32 v17, v17, v129
	v_fma_f32 v17, v17, v161, v49
	v_mul_f32_e32 v17, 4.0, v17
	v_cvt_pk_fp8_f32 v91, v14, v15
	s_nop 0
	v_cvt_pk_fp8_f32 v91, v16, v17 op_sel:[0,0,1]
	global_store_dword v[182:183], v91, off offset:768
	v_mul_f32_e32 v18, v18, v66
	v_mul_f32_e32 v18, v18, v130
	v_fma_f32 v18, v18, v162, v50
	v_mul_f32_e32 v18, 4.0, v18
	v_mul_f32_e32 v19, v19, v66
	v_mul_f32_e32 v19, v19, v131
	v_fma_f32 v19, v19, v163, v51
	v_mul_f32_e32 v19, 4.0, v19
	v_mul_f32_e32 v20, v20, v66
	v_mul_f32_e32 v20, v20, v132
	v_fma_f32 v20, v20, v164, v52
	v_mul_f32_e32 v20, 4.0, v20
	v_mul_f32_e32 v21, v21, v66
	v_mul_f32_e32 v21, v21, v133
	v_fma_f32 v21, v21, v165, v53
	v_mul_f32_e32 v21, 4.0, v21
	v_cvt_pk_fp8_f32 v92, v18, v19
	s_nop 0
	v_cvt_pk_fp8_f32 v92, v20, v21 op_sel:[0,0,1]
	global_store_dword v[182:183], v92, off offset:1024
	v_mul_f32_e32 v22, v22, v66
	v_mul_f32_e32 v22, v22, v134
	v_fma_f32 v22, v22, v166, v54
	v_mul_f32_e32 v22, 4.0, v22
	v_mul_f32_e32 v23, v23, v66
	v_mul_f32_e32 v23, v23, v135
	v_fma_f32 v23, v23, v167, v55
	v_mul_f32_e32 v23, 4.0, v23
	v_mul_f32_e32 v24, v24, v66
	v_mul_f32_e32 v24, v24, v136
	v_fma_f32 v24, v24, v168, v56
	v_mul_f32_e32 v24, 4.0, v24
	v_mul_f32_e32 v25, v25, v66
	v_mul_f32_e32 v25, v25, v137
	v_fma_f32 v25, v25, v169, v57
	v_mul_f32_e32 v25, 4.0, v25
	v_cvt_pk_fp8_f32 v93, v22, v23
	s_nop 0
	v_cvt_pk_fp8_f32 v93, v24, v25 op_sel:[0,0,1]
	global_store_dword v[182:183], v93, off offset:1280
	v_mul_f32_e32 v26, v26, v66
	v_mul_f32_e32 v26, v26, v138
	v_fma_f32 v26, v26, v170, v58
	v_mul_f32_e32 v26, 4.0, v26
	v_mul_f32_e32 v27, v27, v66
	v_mul_f32_e32 v27, v27, v139
	v_fma_f32 v27, v27, v171, v59
	v_mul_f32_e32 v27, 4.0, v27
	v_mul_f32_e32 v28, v28, v66
	v_mul_f32_e32 v28, v28, v140
	v_fma_f32 v28, v28, v172, v60
	v_mul_f32_e32 v28, 4.0, v28
	v_mul_f32_e32 v29, v29, v66
	v_mul_f32_e32 v29, v29, v141
	v_fma_f32 v29, v29, v173, v61
	v_mul_f32_e32 v29, 4.0, v29
	v_cvt_pk_fp8_f32 v91, v26, v27
	s_nop 0
	v_cvt_pk_fp8_f32 v91, v28, v29 op_sel:[0,0,1]
	global_store_dword v[182:183], v91, off offset:1536
	v_mul_f32_e32 v30, v30, v66
	v_mul_f32_e32 v30, v30, v142
	v_fma_f32 v30, v30, v174, v62
	v_mul_f32_e32 v30, 4.0, v30
	v_mul_f32_e32 v31, v31, v66
	v_mul_f32_e32 v31, v31, v143
	v_fma_f32 v31, v31, v175, v63
	v_mul_f32_e32 v31, 4.0, v31
	v_mul_f32_e32 v32, v32, v66
	v_mul_f32_e32 v32, v32, v144
	v_fma_f32 v32, v32, v176, v64
	v_mul_f32_e32 v32, 4.0, v32
	v_mul_f32_e32 v33, v33, v66
	v_mul_f32_e32 v33, v33, v145
	v_fma_f32 v33, v33, v177, v65
	v_mul_f32_e32 v33, 4.0, v33
	v_cvt_pk_fp8_f32 v92, v30, v31
	s_nop 0
	v_cvt_pk_fp8_f32 v92, v32, v33 op_sel:[0,0,1]
	global_store_dword v[182:183], v92, off offset:1792
	s_add_i32 s4, s4, 1
	s_ashr_i32 s5, s4, 31
	s_lshl_b64 s[8:9], s[4:5], 13
	s_lshl_b64 s[14:15], s[4:5], 11
	v_lshl_add_u64 v[178:179], v[68:69], 0, s[8:9]
	v_lshl_add_u64 v[180:181], v[178:179], 0, s[12:13]
	v_lshl_add_u64 v[182:183], v[84:85], 0, s[14:15]
	global_load_dwordx4 v[2:5], v[178:179], off offset:0
	global_load_dwordx4 v[6:9], v[178:179], off offset:1024
	global_load_dwordx4 v[10:13], v[178:179], off offset:2048
	global_load_dwordx4 v[14:17], v[178:179], off offset:3072
	global_load_dwordx4 v[18:21], v[180:181], off offset:0
	global_load_dwordx4 v[22:25], v[180:181], off offset:1024
	global_load_dwordx4 v[26:29], v[180:181], off offset:2048
	global_load_dwordx4 v[30:33], v[180:181], off offset:3072
	s_waitcnt vmcnt(0)
	v_mov_b32_e32 v190, 0
	v_mul_f32_e32 v191, v2, v2
	v_fmac_f32_e32 v191, v3, v3
	v_mul_f32_e32 v192, v4, v4
	v_fmac_f32_e32 v192, v5, v5
	v_add_f32_e32 v191, v191, v192
	v_add_f32_e32 v190, v190, v191
	v_mul_f32_e32 v191, v6, v6
	v_fmac_f32_e32 v191, v7, v7
	v_mul_f32_e32 v192, v8, v8
	v_fmac_f32_e32 v192, v9, v9
	v_add_f32_e32 v191, v191, v192
	v_add_f32_e32 v190, v190, v191
	v_mul_f32_e32 v191, v10, v10
	v_fmac_f32_e32 v191, v11, v11
	v_mul_f32_e32 v192, v12, v12
	v_fmac_f32_e32 v192, v13, v13
	v_add_f32_e32 v191, v191, v192
	v_add_f32_e32 v190, v190, v191
	v_mul_f32_e32 v191, v14, v14
	v_fmac_f32_e32 v191, v15, v15
	v_mul_f32_e32 v192, v16, v16
	v_fmac_f32_e32 v192, v17, v17
	v_add_f32_e32 v191, v191, v192
	v_add_f32_e32 v190, v190, v191
	v_mul_f32_e32 v191, v18, v18
	v_fmac_f32_e32 v191, v19, v19
	v_mul_f32_e32 v192, v20, v20
	v_fmac_f32_e32 v192, v21, v21
	v_add_f32_e32 v191, v191, v192
	v_add_f32_e32 v190, v190, v191
	v_mul_f32_e32 v191, v22, v22
	v_fmac_f32_e32 v191, v23, v23
	v_mul_f32_e32 v192, v24, v24
	v_fmac_f32_e32 v192, v25, v25
	v_add_f32_e32 v191, v191, v192
	v_add_f32_e32 v190, v190, v191
	v_mul_f32_e32 v191, v26, v26
	v_fmac_f32_e32 v191, v27, v27
	v_mul_f32_e32 v192, v28, v28
	v_fmac_f32_e32 v192, v29, v29
	v_add_f32_e32 v191, v191, v192
	v_add_f32_e32 v190, v190, v191
	v_mul_f32_e32 v191, v30, v30
	v_fmac_f32_e32 v191, v31, v31
	v_mul_f32_e32 v192, v32, v32
	v_fmac_f32_e32 v192, v33, v33
	v_add_f32_e32 v191, v191, v192
	v_add_f32_e32 v190, v190, v191
	ds_bpermute_b32 v191, v184, v190
	s_waitcnt lgkmcnt(0)
	v_add_f32_e32 v190, v190, v191
	ds_bpermute_b32 v191, v185, v190
	s_waitcnt lgkmcnt(0)
	v_add_f32_e32 v190, v190, v191
	ds_bpermute_b32 v191, v186, v190
	s_waitcnt lgkmcnt(0)
	v_add_f32_e32 v190, v190, v191
	ds_bpermute_b32 v191, v187, v190
	s_waitcnt lgkmcnt(0)
	v_add_f32_e32 v190, v190, v191
	ds_bpermute_b32 v191, v188, v190
	s_waitcnt lgkmcnt(0)
	v_add_f32_e32 v190, v190, v191
	ds_bpermute_b32 v191, v189, v190
	s_waitcnt lgkmcnt(0)
	v_add_f32_e32 v190, v190, v191
	v_fmamk_f32 v66, v190, 0x3a000000, v100
	v_rsq_f32_e32 v66, v66
	s_nop 0
	v_mul_f32_e32 v2, v2, v66
	v_mul_f32_e32 v2, v2, v114
	v_fma_f32 v2, v2, v146, v34
	v_mul_f32_e32 v2, 4.0, v2
	v_mul_f32_e32 v3, v3, v66
	v_mul_f32_e32 v3, v3, v115
	v_fma_f32 v3, v3, v147, v35
	v_mul_f32_e32 v3, 4.0, v3
	v_mul_f32_e32 v4, v4, v66
	v_mul_f32_e32 v4, v4, v116
	v_fma_f32 v4, v4, v148, v36
	v_mul_f32_e32 v4, 4.0, v4
	v_mul_f32_e32 v5, v5, v66
	v_mul_f32_e32 v5, v5, v117
	v_fma_f32 v5, v5, v149, v37
	v_mul_f32_e32 v5, 4.0, v5
	v_cvt_pk_fp8_f32 v91, v2, v3
	s_nop 0
	v_cvt_pk_fp8_f32 v91, v4, v5 op_sel:[0,0,1]
	global_store_dword v[182:183], v91, off offset:0
	v_mul_f32_e32 v6, v6, v66
	v_mul_f32_e32 v6, v6, v118
	v_fma_f32 v6, v6, v150, v38
	v_mul_f32_e32 v6, 4.0, v6
	v_mul_f32_e32 v7, v7, v66
	v_mul_f32_e32 v7, v7, v119
	v_fma_f32 v7, v7, v151, v39
	v_mul_f32_e32 v7, 4.0, v7
	v_mul_f32_e32 v8, v8, v66
	v_mul_f32_e32 v8, v8, v120
	v_fma_f32 v8, v8, v152, v40
	v_mul_f32_e32 v8, 4.0, v8
	v_mul_f32_e32 v9, v9, v66
	v_mul_f32_e32 v9, v9, v121
	v_fma_f32 v9, v9, v153, v41
	v_mul_f32_e32 v9, 4.0, v9
	v_cvt_pk_fp8_f32 v92, v6, v7
	s_nop 0
	v_cvt_pk_fp8_f32 v92, v8, v9 op_sel:[0,0,1]
	global_store_dword v[182:183], v92, off offset:256
	v_mul_f32_e32 v10, v10, v66
	v_mul_f32_e32 v10, v10, v122
	v_fma_f32 v10, v10, v154, v42
	v_mul_f32_e32 v10, 4.0, v10
	v_mul_f32_e32 v11, v11, v66
	v_mul_f32_e32 v11, v11, v123
	v_fma_f32 v11, v11, v155, v43
	v_mul_f32_e32 v11, 4.0, v11
	v_mul_f32_e32 v12, v12, v66
	v_mul_f32_e32 v12, v12, v124
	v_fma_f32 v12, v12, v156, v44
	v_mul_f32_e32 v12, 4.0, v12
	v_mul_f32_e32 v13, v13, v66
	v_mul_f32_e32 v13, v13, v125
	v_fma_f32 v13, v13, v157, v45
	v_mul_f32_e32 v13, 4.0, v13
	v_cvt_pk_fp8_f32 v93, v10, v11
	s_nop 0
	v_cvt_pk_fp8_f32 v93, v12, v13 op_sel:[0,0,1]
	global_store_dword v[182:183], v93, off offset:512
	v_mul_f32_e32 v14, v14, v66
	v_mul_f32_e32 v14, v14, v126
	v_fma_f32 v14, v14, v158, v46
	v_mul_f32_e32 v14, 4.0, v14
	v_mul_f32_e32 v15, v15, v66
	v_mul_f32_e32 v15, v15, v127
	v_fma_f32 v15, v15, v159, v47
	v_mul_f32_e32 v15, 4.0, v15
	v_mul_f32_e32 v16, v16, v66
	v_mul_f32_e32 v16, v16, v128
	v_fma_f32 v16, v16, v160, v48
	v_mul_f32_e32 v16, 4.0, v16
	v_mul_f32_e32 v17, v17, v66
	v_mul_f32_e32 v17, v17, v129
	v_fma_f32 v17, v17, v161, v49
	v_mul_f32_e32 v17, 4.0, v17
	v_cvt_pk_fp8_f32 v91, v14, v15
	s_nop 0
	v_cvt_pk_fp8_f32 v91, v16, v17 op_sel:[0,0,1]
	global_store_dword v[182:183], v91, off offset:768
	v_mul_f32_e32 v18, v18, v66
	v_mul_f32_e32 v18, v18, v130
	v_fma_f32 v18, v18, v162, v50
	v_mul_f32_e32 v18, 4.0, v18
	v_mul_f32_e32 v19, v19, v66
	v_mul_f32_e32 v19, v19, v131
	v_fma_f32 v19, v19, v163, v51
	v_mul_f32_e32 v19, 4.0, v19
	v_mul_f32_e32 v20, v20, v66
	v_mul_f32_e32 v20, v20, v132
	v_fma_f32 v20, v20, v164, v52
	v_mul_f32_e32 v20, 4.0, v20
	v_mul_f32_e32 v21, v21, v66
	v_mul_f32_e32 v21, v21, v133
	v_fma_f32 v21, v21, v165, v53
	v_mul_f32_e32 v21, 4.0, v21
	v_cvt_pk_fp8_f32 v92, v18, v19
	s_nop 0
	v_cvt_pk_fp8_f32 v92, v20, v21 op_sel:[0,0,1]
	global_store_dword v[182:183], v92, off offset:1024
	v_mul_f32_e32 v22, v22, v66
	v_mul_f32_e32 v22, v22, v134
	v_fma_f32 v22, v22, v166, v54
	v_mul_f32_e32 v22, 4.0, v22
	v_mul_f32_e32 v23, v23, v66
	v_mul_f32_e32 v23, v23, v135
	v_fma_f32 v23, v23, v167, v55
	v_mul_f32_e32 v23, 4.0, v23
	v_mul_f32_e32 v24, v24, v66
	v_mul_f32_e32 v24, v24, v136
	v_fma_f32 v24, v24, v168, v56
	v_mul_f32_e32 v24, 4.0, v24
	v_mul_f32_e32 v25, v25, v66
	v_mul_f32_e32 v25, v25, v137
	v_fma_f32 v25, v25, v169, v57
	v_mul_f32_e32 v25, 4.0, v25
	v_cvt_pk_fp8_f32 v93, v22, v23
	s_nop 0
	v_cvt_pk_fp8_f32 v93, v24, v25 op_sel:[0,0,1]
	global_store_dword v[182:183], v93, off offset:1280
	v_mul_f32_e32 v26, v26, v66
	v_mul_f32_e32 v26, v26, v138
	v_fma_f32 v26, v26, v170, v58
	v_mul_f32_e32 v26, 4.0, v26
	v_mul_f32_e32 v27, v27, v66
	v_mul_f32_e32 v27, v27, v139
	v_fma_f32 v27, v27, v171, v59
	v_mul_f32_e32 v27, 4.0, v27
	v_mul_f32_e32 v28, v28, v66
	v_mul_f32_e32 v28, v28, v140
	v_fma_f32 v28, v28, v172, v60
	v_mul_f32_e32 v28, 4.0, v28
	v_mul_f32_e32 v29, v29, v66
	v_mul_f32_e32 v29, v29, v141
	v_fma_f32 v29, v29, v173, v61
	v_mul_f32_e32 v29, 4.0, v29
	v_cvt_pk_fp8_f32 v91, v26, v27
	s_nop 0
	v_cvt_pk_fp8_f32 v91, v28, v29 op_sel:[0,0,1]
	global_store_dword v[182:183], v91, off offset:1536
	v_mul_f32_e32 v30, v30, v66
	v_mul_f32_e32 v30, v30, v142
	v_fma_f32 v30, v30, v174, v62
	v_mul_f32_e32 v30, 4.0, v30
	v_mul_f32_e32 v31, v31, v66
	v_mul_f32_e32 v31, v31, v143
	v_fma_f32 v31, v31, v175, v63
	v_mul_f32_e32 v31, 4.0, v31
	v_mul_f32_e32 v32, v32, v66
	v_mul_f32_e32 v32, v32, v144
	v_fma_f32 v32, v32, v176, v64
	v_mul_f32_e32 v32, 4.0, v32
	v_mul_f32_e32 v33, v33, v66
	v_mul_f32_e32 v33, v33, v145
	v_fma_f32 v33, v33, v177, v65
	v_mul_f32_e32 v33, 4.0, v33
	v_cvt_pk_fp8_f32 v92, v30, v31
	s_nop 0
	v_cvt_pk_fp8_f32 v92, v32, v33 op_sel:[0,0,1]
	global_store_dword v[182:183], v92, off offset:1792
	s_add_i32 s4, s4, 1
	s_ashr_i32 s5, s4, 31
	s_lshl_b64 s[8:9], s[4:5], 13
	s_lshl_b64 s[14:15], s[4:5], 11
	v_lshl_add_u64 v[178:179], v[68:69], 0, s[8:9]
	v_lshl_add_u64 v[180:181], v[178:179], 0, s[12:13]
	v_lshl_add_u64 v[182:183], v[84:85], 0, s[14:15]
	global_load_dwordx4 v[2:5], v[178:179], off offset:0
	global_load_dwordx4 v[6:9], v[178:179], off offset:1024
	global_load_dwordx4 v[10:13], v[178:179], off offset:2048
	global_load_dwordx4 v[14:17], v[178:179], off offset:3072
	global_load_dwordx4 v[18:21], v[180:181], off offset:0
	global_load_dwordx4 v[22:25], v[180:181], off offset:1024
	global_load_dwordx4 v[26:29], v[180:181], off offset:2048
	global_load_dwordx4 v[30:33], v[180:181], off offset:3072
	s_waitcnt vmcnt(0)
	v_mov_b32_e32 v190, 0
	v_mul_f32_e32 v191, v2, v2
	v_fmac_f32_e32 v191, v3, v3
	v_mul_f32_e32 v192, v4, v4
	v_fmac_f32_e32 v192, v5, v5
	v_add_f32_e32 v191, v191, v192
	v_add_f32_e32 v190, v190, v191
	v_mul_f32_e32 v191, v6, v6
	v_fmac_f32_e32 v191, v7, v7
	v_mul_f32_e32 v192, v8, v8
	v_fmac_f32_e32 v192, v9, v9
	v_add_f32_e32 v191, v191, v192
	v_add_f32_e32 v190, v190, v191
	v_mul_f32_e32 v191, v10, v10
	v_fmac_f32_e32 v191, v11, v11
	v_mul_f32_e32 v192, v12, v12
	v_fmac_f32_e32 v192, v13, v13
	v_add_f32_e32 v191, v191, v192
	v_add_f32_e32 v190, v190, v191
	v_mul_f32_e32 v191, v14, v14
	v_fmac_f32_e32 v191, v15, v15
	v_mul_f32_e32 v192, v16, v16
	v_fmac_f32_e32 v192, v17, v17
	v_add_f32_e32 v191, v191, v192
	v_add_f32_e32 v190, v190, v191
	v_mul_f32_e32 v191, v18, v18
	v_fmac_f32_e32 v191, v19, v19
	v_mul_f32_e32 v192, v20, v20
	v_fmac_f32_e32 v192, v21, v21
	v_add_f32_e32 v191, v191, v192
	v_add_f32_e32 v190, v190, v191
	v_mul_f32_e32 v191, v22, v22
	v_fmac_f32_e32 v191, v23, v23
	v_mul_f32_e32 v192, v24, v24
	v_fmac_f32_e32 v192, v25, v25
	v_add_f32_e32 v191, v191, v192
	v_add_f32_e32 v190, v190, v191
	v_mul_f32_e32 v191, v26, v26
	v_fmac_f32_e32 v191, v27, v27
	v_mul_f32_e32 v192, v28, v28
	v_fmac_f32_e32 v192, v29, v29
	v_add_f32_e32 v191, v191, v192
	v_add_f32_e32 v190, v190, v191
	v_mul_f32_e32 v191, v30, v30
	v_fmac_f32_e32 v191, v31, v31
	v_mul_f32_e32 v192, v32, v32
	v_fmac_f32_e32 v192, v33, v33
	v_add_f32_e32 v191, v191, v192
	v_add_f32_e32 v190, v190, v191
	ds_bpermute_b32 v191, v184, v190
	s_waitcnt lgkmcnt(0)
	v_add_f32_e32 v190, v190, v191
	ds_bpermute_b32 v191, v185, v190
	s_waitcnt lgkmcnt(0)
	v_add_f32_e32 v190, v190, v191
	ds_bpermute_b32 v191, v186, v190
	s_waitcnt lgkmcnt(0)
	v_add_f32_e32 v190, v190, v191
	ds_bpermute_b32 v191, v187, v190
	s_waitcnt lgkmcnt(0)
	v_add_f32_e32 v190, v190, v191
	ds_bpermute_b32 v191, v188, v190
	s_waitcnt lgkmcnt(0)
	v_add_f32_e32 v190, v190, v191
	ds_bpermute_b32 v191, v189, v190
	s_waitcnt lgkmcnt(0)
	v_add_f32_e32 v190, v190, v191
	v_fmamk_f32 v66, v190, 0x3a000000, v100
	v_rsq_f32_e32 v66, v66
	s_nop 0
	v_mul_f32_e32 v2, v2, v66
	v_mul_f32_e32 v2, v2, v114
	v_fma_f32 v2, v2, v146, v34
	v_mul_f32_e32 v2, 4.0, v2
	v_mul_f32_e32 v3, v3, v66
	v_mul_f32_e32 v3, v3, v115
	v_fma_f32 v3, v3, v147, v35
	v_mul_f32_e32 v3, 4.0, v3
	v_mul_f32_e32 v4, v4, v66
	v_mul_f32_e32 v4, v4, v116
	v_fma_f32 v4, v4, v148, v36
	v_mul_f32_e32 v4, 4.0, v4
	v_mul_f32_e32 v5, v5, v66
	v_mul_f32_e32 v5, v5, v117
	v_fma_f32 v5, v5, v149, v37
	v_mul_f32_e32 v5, 4.0, v5
	v_cvt_pk_fp8_f32 v91, v2, v3
	s_nop 0
	v_cvt_pk_fp8_f32 v91, v4, v5 op_sel:[0,0,1]
	global_store_dword v[182:183], v91, off offset:0
	v_mul_f32_e32 v6, v6, v66
	v_mul_f32_e32 v6, v6, v118
	v_fma_f32 v6, v6, v150, v38
	v_mul_f32_e32 v6, 4.0, v6
	v_mul_f32_e32 v7, v7, v66
	v_mul_f32_e32 v7, v7, v119
	v_fma_f32 v7, v7, v151, v39
	v_mul_f32_e32 v7, 4.0, v7
	v_mul_f32_e32 v8, v8, v66
	v_mul_f32_e32 v8, v8, v120
	v_fma_f32 v8, v8, v152, v40
	v_mul_f32_e32 v8, 4.0, v8
	v_mul_f32_e32 v9, v9, v66
	v_mul_f32_e32 v9, v9, v121
	v_fma_f32 v9, v9, v153, v41
	v_mul_f32_e32 v9, 4.0, v9
	v_cvt_pk_fp8_f32 v92, v6, v7
	s_nop 0
	v_cvt_pk_fp8_f32 v92, v8, v9 op_sel:[0,0,1]
	global_store_dword v[182:183], v92, off offset:256
	v_mul_f32_e32 v10, v10, v66
	v_mul_f32_e32 v10, v10, v122
	v_fma_f32 v10, v10, v154, v42
	v_mul_f32_e32 v10, 4.0, v10
	v_mul_f32_e32 v11, v11, v66
	v_mul_f32_e32 v11, v11, v123
	v_fma_f32 v11, v11, v155, v43
	v_mul_f32_e32 v11, 4.0, v11
	v_mul_f32_e32 v12, v12, v66
	v_mul_f32_e32 v12, v12, v124
	v_fma_f32 v12, v12, v156, v44
	v_mul_f32_e32 v12, 4.0, v12
	v_mul_f32_e32 v13, v13, v66
	v_mul_f32_e32 v13, v13, v125
	v_fma_f32 v13, v13, v157, v45
	v_mul_f32_e32 v13, 4.0, v13
	v_cvt_pk_fp8_f32 v93, v10, v11
	s_nop 0
	v_cvt_pk_fp8_f32 v93, v12, v13 op_sel:[0,0,1]
	global_store_dword v[182:183], v93, off offset:512
	v_mul_f32_e32 v14, v14, v66
	v_mul_f32_e32 v14, v14, v126
	v_fma_f32 v14, v14, v158, v46
	v_mul_f32_e32 v14, 4.0, v14
	v_mul_f32_e32 v15, v15, v66
	v_mul_f32_e32 v15, v15, v127
	v_fma_f32 v15, v15, v159, v47
	v_mul_f32_e32 v15, 4.0, v15
	v_mul_f32_e32 v16, v16, v66
	v_mul_f32_e32 v16, v16, v128
	v_fma_f32 v16, v16, v160, v48
	v_mul_f32_e32 v16, 4.0, v16
	v_mul_f32_e32 v17, v17, v66
	v_mul_f32_e32 v17, v17, v129
	v_fma_f32 v17, v17, v161, v49
	v_mul_f32_e32 v17, 4.0, v17
	v_cvt_pk_fp8_f32 v91, v14, v15
	s_nop 0
	v_cvt_pk_fp8_f32 v91, v16, v17 op_sel:[0,0,1]
	global_store_dword v[182:183], v91, off offset:768
	v_mul_f32_e32 v18, v18, v66
	v_mul_f32_e32 v18, v18, v130
	v_fma_f32 v18, v18, v162, v50
	v_mul_f32_e32 v18, 4.0, v18
	v_mul_f32_e32 v19, v19, v66
	v_mul_f32_e32 v19, v19, v131
	v_fma_f32 v19, v19, v163, v51
	v_mul_f32_e32 v19, 4.0, v19
	v_mul_f32_e32 v20, v20, v66
	v_mul_f32_e32 v20, v20, v132
	v_fma_f32 v20, v20, v164, v52
	v_mul_f32_e32 v20, 4.0, v20
	v_mul_f32_e32 v21, v21, v66
	v_mul_f32_e32 v21, v21, v133
	v_fma_f32 v21, v21, v165, v53
	v_mul_f32_e32 v21, 4.0, v21
	v_cvt_pk_fp8_f32 v92, v18, v19
	s_nop 0
	v_cvt_pk_fp8_f32 v92, v20, v21 op_sel:[0,0,1]
	global_store_dword v[182:183], v92, off offset:1024
	v_mul_f32_e32 v22, v22, v66
	v_mul_f32_e32 v22, v22, v134
	v_fma_f32 v22, v22, v166, v54
	v_mul_f32_e32 v22, 4.0, v22
	v_mul_f32_e32 v23, v23, v66
	v_mul_f32_e32 v23, v23, v135
	v_fma_f32 v23, v23, v167, v55
	v_mul_f32_e32 v23, 4.0, v23
	v_mul_f32_e32 v24, v24, v66
	v_mul_f32_e32 v24, v24, v136
	v_fma_f32 v24, v24, v168, v56
	v_mul_f32_e32 v24, 4.0, v24
	v_mul_f32_e32 v25, v25, v66
	v_mul_f32_e32 v25, v25, v137
	v_fma_f32 v25, v25, v169, v57
	v_mul_f32_e32 v25, 4.0, v25
	v_cvt_pk_fp8_f32 v93, v22, v23
	s_nop 0
	v_cvt_pk_fp8_f32 v93, v24, v25 op_sel:[0,0,1]
	global_store_dword v[182:183], v93, off offset:1280
	v_mul_f32_e32 v26, v26, v66
	v_mul_f32_e32 v26, v26, v138
	v_fma_f32 v26, v26, v170, v58
	v_mul_f32_e32 v26, 4.0, v26
	v_mul_f32_e32 v27, v27, v66
	v_mul_f32_e32 v27, v27, v139
	v_fma_f32 v27, v27, v171, v59
	v_mul_f32_e32 v27, 4.0, v27
	v_mul_f32_e32 v28, v28, v66
	v_mul_f32_e32 v28, v28, v140
	v_fma_f32 v28, v28, v172, v60
	v_mul_f32_e32 v28, 4.0, v28
	v_mul_f32_e32 v29, v29, v66
	v_mul_f32_e32 v29, v29, v141
	v_fma_f32 v29, v29, v173, v61
	v_mul_f32_e32 v29, 4.0, v29
	v_cvt_pk_fp8_f32 v91, v26, v27
	s_nop 0
	v_cvt_pk_fp8_f32 v91, v28, v29 op_sel:[0,0,1]
	global_store_dword v[182:183], v91, off offset:1536
	v_mul_f32_e32 v30, v30, v66
	v_mul_f32_e32 v30, v30, v142
	v_fma_f32 v30, v30, v174, v62
	v_mul_f32_e32 v30, 4.0, v30
	v_mul_f32_e32 v31, v31, v66
	v_mul_f32_e32 v31, v31, v143
	v_fma_f32 v31, v31, v175, v63
	v_mul_f32_e32 v31, 4.0, v31
	v_mul_f32_e32 v32, v32, v66
	v_mul_f32_e32 v32, v32, v144
	v_fma_f32 v32, v32, v176, v64
	v_mul_f32_e32 v32, 4.0, v32
	v_mul_f32_e32 v33, v33, v66
	v_mul_f32_e32 v33, v33, v145
	v_fma_f32 v33, v33, v177, v65
	v_mul_f32_e32 v33, 4.0, v33
	v_cvt_pk_fp8_f32 v92, v30, v31
	s_nop 0
	v_cvt_pk_fp8_f32 v92, v32, v33 op_sel:[0,0,1]
	global_store_dword v[182:183], v92, off offset:1792
	s_add_i32 s4, s4, 1
	s_ashr_i32 s5, s4, 31
	s_lshl_b64 s[8:9], s[4:5], 13
	s_lshl_b64 s[14:15], s[4:5], 11
	v_lshl_add_u64 v[178:179], v[68:69], 0, s[8:9]
	v_lshl_add_u64 v[180:181], v[178:179], 0, s[12:13]
	v_lshl_add_u64 v[182:183], v[84:85], 0, s[14:15]
	global_load_dwordx4 v[2:5], v[178:179], off offset:0
	global_load_dwordx4 v[6:9], v[178:179], off offset:1024
	global_load_dwordx4 v[10:13], v[178:179], off offset:2048
	global_load_dwordx4 v[14:17], v[178:179], off offset:3072
	global_load_dwordx4 v[18:21], v[180:181], off offset:0
	global_load_dwordx4 v[22:25], v[180:181], off offset:1024
	global_load_dwordx4 v[26:29], v[180:181], off offset:2048
	global_load_dwordx4 v[30:33], v[180:181], off offset:3072
	s_waitcnt vmcnt(0)
	v_mov_b32_e32 v190, 0
	v_mul_f32_e32 v191, v2, v2
	v_fmac_f32_e32 v191, v3, v3
	v_mul_f32_e32 v192, v4, v4
	v_fmac_f32_e32 v192, v5, v5
	v_add_f32_e32 v191, v191, v192
	v_add_f32_e32 v190, v190, v191
	v_mul_f32_e32 v191, v6, v6
	v_fmac_f32_e32 v191, v7, v7
	v_mul_f32_e32 v192, v8, v8
	v_fmac_f32_e32 v192, v9, v9
	v_add_f32_e32 v191, v191, v192
	v_add_f32_e32 v190, v190, v191
	v_mul_f32_e32 v191, v10, v10
	v_fmac_f32_e32 v191, v11, v11
	v_mul_f32_e32 v192, v12, v12
	v_fmac_f32_e32 v192, v13, v13
	v_add_f32_e32 v191, v191, v192
	v_add_f32_e32 v190, v190, v191
	v_mul_f32_e32 v191, v14, v14
	v_fmac_f32_e32 v191, v15, v15
	v_mul_f32_e32 v192, v16, v16
	v_fmac_f32_e32 v192, v17, v17
	v_add_f32_e32 v191, v191, v192
	v_add_f32_e32 v190, v190, v191
	v_mul_f32_e32 v191, v18, v18
	v_fmac_f32_e32 v191, v19, v19
	v_mul_f32_e32 v192, v20, v20
	v_fmac_f32_e32 v192, v21, v21
	v_add_f32_e32 v191, v191, v192
	v_add_f32_e32 v190, v190, v191
	v_mul_f32_e32 v191, v22, v22
	v_fmac_f32_e32 v191, v23, v23
	v_mul_f32_e32 v192, v24, v24
	v_fmac_f32_e32 v192, v25, v25
	v_add_f32_e32 v191, v191, v192
	v_add_f32_e32 v190, v190, v191
	v_mul_f32_e32 v191, v26, v26
	v_fmac_f32_e32 v191, v27, v27
	v_mul_f32_e32 v192, v28, v28
	v_fmac_f32_e32 v192, v29, v29
	v_add_f32_e32 v191, v191, v192
	v_add_f32_e32 v190, v190, v191
	v_mul_f32_e32 v191, v30, v30
	v_fmac_f32_e32 v191, v31, v31
	v_mul_f32_e32 v192, v32, v32
	v_fmac_f32_e32 v192, v33, v33
	v_add_f32_e32 v191, v191, v192
	v_add_f32_e32 v190, v190, v191
	ds_bpermute_b32 v191, v184, v190
	s_waitcnt lgkmcnt(0)
	v_add_f32_e32 v190, v190, v191
	ds_bpermute_b32 v191, v185, v190
	s_waitcnt lgkmcnt(0)
	v_add_f32_e32 v190, v190, v191
	ds_bpermute_b32 v191, v186, v190
	s_waitcnt lgkmcnt(0)
	v_add_f32_e32 v190, v190, v191
	ds_bpermute_b32 v191, v187, v190
	s_waitcnt lgkmcnt(0)
	v_add_f32_e32 v190, v190, v191
	ds_bpermute_b32 v191, v188, v190
	s_waitcnt lgkmcnt(0)
	v_add_f32_e32 v190, v190, v191
	ds_bpermute_b32 v191, v189, v190
	s_waitcnt lgkmcnt(0)
	v_add_f32_e32 v190, v190, v191
	v_fmamk_f32 v66, v190, 0x3a000000, v100
	v_rsq_f32_e32 v66, v66
	s_nop 0
	v_mul_f32_e32 v2, v2, v66
	v_mul_f32_e32 v2, v2, v114
	v_fma_f32 v2, v2, v146, v34
	v_mul_f32_e32 v2, 4.0, v2
	v_mul_f32_e32 v3, v3, v66
	v_mul_f32_e32 v3, v3, v115
	v_fma_f32 v3, v3, v147, v35
	v_mul_f32_e32 v3, 4.0, v3
	v_mul_f32_e32 v4, v4, v66
	v_mul_f32_e32 v4, v4, v116
	v_fma_f32 v4, v4, v148, v36
	v_mul_f32_e32 v4, 4.0, v4
	v_mul_f32_e32 v5, v5, v66
	v_mul_f32_e32 v5, v5, v117
	v_fma_f32 v5, v5, v149, v37
	v_mul_f32_e32 v5, 4.0, v5
	v_cvt_pk_fp8_f32 v91, v2, v3
	s_nop 0
	v_cvt_pk_fp8_f32 v91, v4, v5 op_sel:[0,0,1]
	global_store_dword v[182:183], v91, off offset:0
	v_mul_f32_e32 v6, v6, v66
	v_mul_f32_e32 v6, v6, v118
	v_fma_f32 v6, v6, v150, v38
	v_mul_f32_e32 v6, 4.0, v6
	v_mul_f32_e32 v7, v7, v66
	v_mul_f32_e32 v7, v7, v119
	v_fma_f32 v7, v7, v151, v39
	v_mul_f32_e32 v7, 4.0, v7
	v_mul_f32_e32 v8, v8, v66
	v_mul_f32_e32 v8, v8, v120
	v_fma_f32 v8, v8, v152, v40
	v_mul_f32_e32 v8, 4.0, v8
	v_mul_f32_e32 v9, v9, v66
	v_mul_f32_e32 v9, v9, v121
	v_fma_f32 v9, v9, v153, v41
	v_mul_f32_e32 v9, 4.0, v9
	v_cvt_pk_fp8_f32 v92, v6, v7
	s_nop 0
	v_cvt_pk_fp8_f32 v92, v8, v9 op_sel:[0,0,1]
	global_store_dword v[182:183], v92, off offset:256
	v_mul_f32_e32 v10, v10, v66
	v_mul_f32_e32 v10, v10, v122
	v_fma_f32 v10, v10, v154, v42
	v_mul_f32_e32 v10, 4.0, v10
	v_mul_f32_e32 v11, v11, v66
	v_mul_f32_e32 v11, v11, v123
	v_fma_f32 v11, v11, v155, v43
	v_mul_f32_e32 v11, 4.0, v11
	v_mul_f32_e32 v12, v12, v66
	v_mul_f32_e32 v12, v12, v124
	v_fma_f32 v12, v12, v156, v44
	v_mul_f32_e32 v12, 4.0, v12
	v_mul_f32_e32 v13, v13, v66
	v_mul_f32_e32 v13, v13, v125
	v_fma_f32 v13, v13, v157, v45
	v_mul_f32_e32 v13, 4.0, v13
	v_cvt_pk_fp8_f32 v93, v10, v11
	s_nop 0
	v_cvt_pk_fp8_f32 v93, v12, v13 op_sel:[0,0,1]
	global_store_dword v[182:183], v93, off offset:512
	v_mul_f32_e32 v14, v14, v66
	v_mul_f32_e32 v14, v14, v126
	v_fma_f32 v14, v14, v158, v46
	v_mul_f32_e32 v14, 4.0, v14
	v_mul_f32_e32 v15, v15, v66
	v_mul_f32_e32 v15, v15, v127
	v_fma_f32 v15, v15, v159, v47
	v_mul_f32_e32 v15, 4.0, v15
	v_mul_f32_e32 v16, v16, v66
	v_mul_f32_e32 v16, v16, v128
	v_fma_f32 v16, v16, v160, v48
	v_mul_f32_e32 v16, 4.0, v16
	v_mul_f32_e32 v17, v17, v66
	v_mul_f32_e32 v17, v17, v129
	v_fma_f32 v17, v17, v161, v49
	v_mul_f32_e32 v17, 4.0, v17
	v_cvt_pk_fp8_f32 v91, v14, v15
	s_nop 0
	v_cvt_pk_fp8_f32 v91, v16, v17 op_sel:[0,0,1]
	global_store_dword v[182:183], v91, off offset:768
	v_mul_f32_e32 v18, v18, v66
	v_mul_f32_e32 v18, v18, v130
	v_fma_f32 v18, v18, v162, v50
	v_mul_f32_e32 v18, 4.0, v18
	v_mul_f32_e32 v19, v19, v66
	v_mul_f32_e32 v19, v19, v131
	v_fma_f32 v19, v19, v163, v51
	v_mul_f32_e32 v19, 4.0, v19
	v_mul_f32_e32 v20, v20, v66
	v_mul_f32_e32 v20, v20, v132
	v_fma_f32 v20, v20, v164, v52
	v_mul_f32_e32 v20, 4.0, v20
	v_mul_f32_e32 v21, v21, v66
	v_mul_f32_e32 v21, v21, v133
	v_fma_f32 v21, v21, v165, v53
	v_mul_f32_e32 v21, 4.0, v21
	v_cvt_pk_fp8_f32 v92, v18, v19
	s_nop 0
	v_cvt_pk_fp8_f32 v92, v20, v21 op_sel:[0,0,1]
	global_store_dword v[182:183], v92, off offset:1024
	v_mul_f32_e32 v22, v22, v66
	v_mul_f32_e32 v22, v22, v134
	v_fma_f32 v22, v22, v166, v54
	v_mul_f32_e32 v22, 4.0, v22
	v_mul_f32_e32 v23, v23, v66
	v_mul_f32_e32 v23, v23, v135
	v_fma_f32 v23, v23, v167, v55
	v_mul_f32_e32 v23, 4.0, v23
	v_mul_f32_e32 v24, v24, v66
	v_mul_f32_e32 v24, v24, v136
	v_fma_f32 v24, v24, v168, v56
	v_mul_f32_e32 v24, 4.0, v24
	v_mul_f32_e32 v25, v25, v66
	v_mul_f32_e32 v25, v25, v137
	v_fma_f32 v25, v25, v169, v57
	v_mul_f32_e32 v25, 4.0, v25
	v_cvt_pk_fp8_f32 v93, v22, v23
	s_nop 0
	v_cvt_pk_fp8_f32 v93, v24, v25 op_sel:[0,0,1]
	global_store_dword v[182:183], v93, off offset:1280
	v_mul_f32_e32 v26, v26, v66
	v_mul_f32_e32 v26, v26, v138
	v_fma_f32 v26, v26, v170, v58
	v_mul_f32_e32 v26, 4.0, v26
	v_mul_f32_e32 v27, v27, v66
	v_mul_f32_e32 v27, v27, v139
	v_fma_f32 v27, v27, v171, v59
	v_mul_f32_e32 v27, 4.0, v27
	v_mul_f32_e32 v28, v28, v66
	v_mul_f32_e32 v28, v28, v140
	v_fma_f32 v28, v28, v172, v60
	v_mul_f32_e32 v28, 4.0, v28
	v_mul_f32_e32 v29, v29, v66
	v_mul_f32_e32 v29, v29, v141
	v_fma_f32 v29, v29, v173, v61
	v_mul_f32_e32 v29, 4.0, v29
	v_cvt_pk_fp8_f32 v91, v26, v27
	s_nop 0
	v_cvt_pk_fp8_f32 v91, v28, v29 op_sel:[0,0,1]
	global_store_dword v[182:183], v91, off offset:1536
	v_mul_f32_e32 v30, v30, v66
	v_mul_f32_e32 v30, v30, v142
	v_fma_f32 v30, v30, v174, v62
	v_mul_f32_e32 v30, 4.0, v30
	v_mul_f32_e32 v31, v31, v66
	v_mul_f32_e32 v31, v31, v143
	v_fma_f32 v31, v31, v175, v63
	v_mul_f32_e32 v31, 4.0, v31
	v_mul_f32_e32 v32, v32, v66
	v_mul_f32_e32 v32, v32, v144
	v_fma_f32 v32, v32, v176, v64
	v_mul_f32_e32 v32, 4.0, v32
	v_mul_f32_e32 v33, v33, v66
	v_mul_f32_e32 v33, v33, v145
	v_fma_f32 v33, v33, v177, v65
	v_mul_f32_e32 v33, 4.0, v33
	v_cvt_pk_fp8_f32 v92, v30, v31
	s_nop 0
	v_cvt_pk_fp8_f32 v92, v32, v33 op_sel:[0,0,1]
	global_store_dword v[182:183], v92, off offset:1792
	v_readlane_b32 s0, v249, 12
	s_add_i32 s94, s94, s0
	s_cmpk_lt_i32 s94, 0x100
	v_readlane_b32 s1, v249, 13
	s_barrier
	s_cbranch_scc0 .LBB0_1302

.LBB0_1572:
	v_readlane_b32 s2, v249, 14
	v_readlane_b32 s3, v249, 15
	s_cmp_lt_i32 s2, 12
	s_cselect_b64 s[2:3], -1, 0
	s_and_b64 s[0:1], s[2:3], s[0:1]
	s_andn2_b64 vcc, exec, s[0:1]
	s_cbranch_vccnz .LBB0_1576
	v_readlane_b32 s0, v249, 0
	s_lshl_b32 s0, s0, 3
	s_add_i32 s2, s0, s92
	s_cmpk_gt_i32 s2, 0x1fff
	v_readlane_b32 s1, v249, 1
	s_cbranch_scc1 .LBB0_1576
	s_waitcnt lgkmcnt(0)
	v_readlane_b32 s4, v249, 12
	s_lshl_b32 s4, s4, 3
	v_readlane_b32 s18, v249, 6
	v_readlane_b32 s19, v249, 7
	v_readlane_b32 s24, v249, 8
	v_readlane_b32 s25, v249, 9
	v_mov_b32_e32 v1, 0
	v_lshlrev_b32_e32 v2, 4, v222
	v_lshlrev_b32_e32 v3, 2, v222
	v_xor_b32_e32 v224, 1, v222
	v_lshlrev_b32_e32 v224, 2, v224
	v_xor_b32_e32 v225, 2, v222
	v_lshlrev_b32_e32 v225, 2, v225
	v_xor_b32_e32 v226, 4, v222
	v_lshlrev_b32_e32 v226, 2, v226
	v_xor_b32_e32 v227, 8, v222
	v_lshlrev_b32_e32 v227, 2, v227
	v_xor_b32_e32 v228, 16, v222
	v_lshlrev_b32_e32 v228, 2, v228
	v_xor_b32_e32 v229, 32, v222
	v_lshlrev_b32_e32 v229, 2, v229
	s_add_u32 s14, s50, 0x94800000
	s_addc_u32 s15, s51, 0
	s_mov_b32 s26, -1
	s_mov_b32 s40, 0x3d800000
	s_mov_b32 s41, 0x3a000000
	s_mov_b32 s42, 0x358637bd
.Lp11_row:
	s_lshr_b32 s27, s2, 12
	s_lshl_b32 s28, s2, 13
	s_add_u32 s6, s50, 0x50800000
	s_addc_u32 s7, s51, 0
	s_add_u32 s6, s6, s28
	s_addc_u32 s7, s7, 0
	s_add_u32 s30, s6, 0x1000
	s_addc_u32 s31, s7, 0
	s_add_u32 s8, s24, s28
	s_addc_u32 s9, s25, 0
	s_add_u32 s32, s8, 0x1000
	s_addc_u32 s33, s9, 0
	s_lshl_b32 s29, s2, 4
	s_add_u32 s10, s50, 0x400000
	s_addc_u32 s11, s51, 0
	s_add_u32 s10, s10, s29
	s_addc_u32 s11, s11, 0
	s_add_u32 s12, s10, 0x40000
	s_addc_u32 s13, s11, 0
	global_load_dwordx4 v[4:7], v1, s[10:11]
	global_load_dwordx4 v[8:11], v1, s[12:13]
	global_load_dwordx4 v[32:35], v2, s[6:7] offset:0 nt
	global_load_dwordx4 v[36:39], v2, s[6:7] offset:1024 nt
	global_load_dwordx4 v[40:43], v2, s[6:7] offset:2048 nt
	global_load_dwordx4 v[44:47], v2, s[6:7] offset:3072 nt
	global_load_dwordx4 v[48:51], v2, s[30:31] offset:0 nt
	global_load_dwordx4 v[52:55], v2, s[30:31] offset:1024 nt
	global_load_dwordx4 v[56:59], v2, s[30:31] offset:2048 nt
	global_load_dwordx4 v[60:63], v2, s[30:31] offset:3072 nt
	s_cmp_eq_u32 s26, s27
	s_cbranch_scc1 .Lp11_samegf
	s_mul_i32 s34, s27, 0xc000
	s_add_u32 s16, s50, 0x8a000
	s_addc_u32 s17, s51, 0
	s_add_u32 s16, s16, s34
	s_addc_u32 s17, s17, 0
	s_add_u32 s34, s16, 0x1000
	s_addc_u32 s35, s17, 0
	global_load_dwordx4 v[96:99], v2, s[16:17] offset:0
	global_load_dwordx4 v[100:103], v2, s[16:17] offset:1024
	global_load_dwordx4 v[104:107], v2, s[16:17] offset:2048
	global_load_dwordx4 v[108:111], v2, s[16:17] offset:3072
	global_load_dwordx4 v[112:115], v2, s[34:35] offset:0
	global_load_dwordx4 v[116:119], v2, s[34:35] offset:1024
	global_load_dwordx4 v[120:123], v2, s[34:35] offset:2048
	global_load_dwordx4 v[124:127], v2, s[34:35] offset:3072
	s_waitcnt vmcnt(16)
	s_branch .Lp11_gotti
.Lp11_samegf:
	s_waitcnt vmcnt(8)
.Lp11_gotti:
	v_lshl_add_u32 v12, v4, 11, v3
	v_lshl_add_u32 v13, v5, 11, v3
	v_lshl_add_u32 v14, v6, 11, v3
	v_lshl_add_u32 v15, v7, 11, v3
	global_load_dword v64, v12, s[14:15] offset:0 nt
	global_load_dword v65, v13, s[14:15] offset:0 nt
	global_load_dword v66, v14, s[14:15] offset:0 nt
	global_load_dword v67, v15, s[14:15] offset:0 nt
	global_load_dword v68, v12, s[14:15] offset:256 nt
	global_load_dword v69, v13, s[14:15] offset:256 nt
	global_load_dword v70, v14, s[14:15] offset:256 nt
	global_load_dword v71, v15, s[14:15] offset:256 nt
	global_load_dword v72, v12, s[14:15] offset:512 nt
	global_load_dword v73, v13, s[14:15] offset:512 nt
	global_load_dword v74, v14, s[14:15] offset:512 nt
	global_load_dword v75, v15, s[14:15] offset:512 nt
	global_load_dword v76, v12, s[14:15] offset:768 nt
	global_load_dword v77, v13, s[14:15] offset:768 nt
	global_load_dword v78, v14, s[14:15] offset:768 nt
	global_load_dword v79, v15, s[14:15] offset:768 nt
	global_load_dword v80, v12, s[14:15] offset:1024 nt
	global_load_dword v81, v13, s[14:15] offset:1024 nt
	global_load_dword v82, v14, s[14:15] offset:1024 nt
	global_load_dword v83, v15, s[14:15] offset:1024 nt
	global_load_dword v84, v12, s[14:15] offset:1280 nt
	global_load_dword v85, v13, s[14:15] offset:1280 nt
	global_load_dword v86, v14, s[14:15] offset:1280 nt
	global_load_dword v87, v15, s[14:15] offset:1280 nt
	global_load_dword v88, v12, s[14:15] offset:1536 nt
	global_load_dword v89, v13, s[14:15] offset:1536 nt
	global_load_dword v90, v14, s[14:15] offset:1536 nt
	global_load_dword v91, v15, s[14:15] offset:1536 nt
	global_load_dword v92, v12, s[14:15] offset:1792 nt
	global_load_dword v93, v13, s[14:15] offset:1792 nt
	global_load_dword v94, v14, s[14:15] offset:1792 nt
	global_load_dword v95, v15, s[14:15] offset:1792 nt
	v_mul_f32_e32 v16, s40, v8
	v_mul_f32_e32 v17, s40, v9
	v_mul_f32_e32 v18, s40, v10
	v_mul_f32_e32 v19, s40, v11
	s_nop 0
	v_readfirstlane_b32 s36, v16
	v_readfirstlane_b32 s37, v17
	v_readfirstlane_b32 s38, v18
	v_readfirstlane_b32 s39, v19
	v_mov_b32_e32 v230, 0
	s_waitcnt vmcnt(0)
	v_cvt_pk_f32_fp8_e32 v[16:17], v64
	v_cvt_pk_f32_fp8_sdwa v[24:25], v64 src0_sel:WORD_1
	v_cvt_pk_f32_fp8_e32 v[18:19], v65
	v_cvt_pk_f32_fp8_sdwa v[26:27], v65 src0_sel:WORD_1
	v_cvt_pk_f32_fp8_e32 v[20:21], v66
	v_cvt_pk_f32_fp8_sdwa v[28:29], v66 src0_sel:WORD_1
	v_cvt_pk_f32_fp8_e32 v[22:23], v67
	v_cvt_pk_f32_fp8_sdwa v[30:31], v67 src0_sel:WORD_1
	v_mul_f32_e32 v231, s37, v18
	v_fmac_f32_e32 v231, s36, v16
	v_fmac_f32_e32 v231, s38, v20
	v_fmac_f32_e32 v231, s39, v22
	v_fmac_f32_e32 v32, v96, v231
	v_mul_f32_e32 v231, s37, v19
	v_fmac_f32_e32 v231, s36, v17
	v_fmac_f32_e32 v231, s38, v21
	v_fmac_f32_e32 v231, s39, v23
	v_fmac_f32_e32 v33, v97, v231
	v_mul_f32_e32 v231, s37, v26
	v_fmac_f32_e32 v231, s36, v24
	v_fmac_f32_e32 v231, s38, v28
	v_fmac_f32_e32 v231, s39, v30
	v_fmac_f32_e32 v34, v98, v231
	v_mul_f32_e32 v231, s37, v27
	v_fmac_f32_e32 v231, s36, v25
	v_fmac_f32_e32 v231, s38, v29
	v_fmac_f32_e32 v231, s39, v31
	v_fmac_f32_e32 v35, v99, v231
	v_mul_f32_e32 v232, v32, v32
	v_fmac_f32_e32 v232, v33, v33
	v_mul_f32_e32 v233, v34, v34
	v_fmac_f32_e32 v233, v35, v35
	v_add_f32_e32 v232, v232, v233
	v_add_f32_e32 v230, v230, v232
	v_cvt_pk_f32_fp8_e32 v[16:17], v68
	v_cvt_pk_f32_fp8_sdwa v[24:25], v68 src0_sel:WORD_1
	v_cvt_pk_f32_fp8_e32 v[18:19], v69
	v_cvt_pk_f32_fp8_sdwa v[26:27], v69 src0_sel:WORD_1
	v_cvt_pk_f32_fp8_e32 v[20:21], v70
	v_cvt_pk_f32_fp8_sdwa v[28:29], v70 src0_sel:WORD_1
	v_cvt_pk_f32_fp8_e32 v[22:23], v71
	v_cvt_pk_f32_fp8_sdwa v[30:31], v71 src0_sel:WORD_1
	v_mul_f32_e32 v231, s37, v18
	v_fmac_f32_e32 v231, s36, v16
	v_fmac_f32_e32 v231, s38, v20
	v_fmac_f32_e32 v231, s39, v22
	v_fmac_f32_e32 v36, v100, v231
	v_mul_f32_e32 v231, s37, v19
	v_fmac_f32_e32 v231, s36, v17
	v_fmac_f32_e32 v231, s38, v21
	v_fmac_f32_e32 v231, s39, v23
	v_fmac_f32_e32 v37, v101, v231
	v_mul_f32_e32 v231, s37, v26
	v_fmac_f32_e32 v231, s36, v24
	v_fmac_f32_e32 v231, s38, v28
	v_fmac_f32_e32 v231, s39, v30
	v_fmac_f32_e32 v38, v102, v231
	v_mul_f32_e32 v231, s37, v27
	v_fmac_f32_e32 v231, s36, v25
	v_fmac_f32_e32 v231, s38, v29
	v_fmac_f32_e32 v231, s39, v31
	v_fmac_f32_e32 v39, v103, v231
	v_mul_f32_e32 v232, v36, v36
	v_fmac_f32_e32 v232, v37, v37
	v_mul_f32_e32 v233, v38, v38
	v_fmac_f32_e32 v233, v39, v39
	v_add_f32_e32 v232, v232, v233
	v_add_f32_e32 v230, v230, v232
	v_cvt_pk_f32_fp8_e32 v[16:17], v72
	v_cvt_pk_f32_fp8_sdwa v[24:25], v72 src0_sel:WORD_1
	v_cvt_pk_f32_fp8_e32 v[18:19], v73
	v_cvt_pk_f32_fp8_sdwa v[26:27], v73 src0_sel:WORD_1
	v_cvt_pk_f32_fp8_e32 v[20:21], v74
	v_cvt_pk_f32_fp8_sdwa v[28:29], v74 src0_sel:WORD_1
	v_cvt_pk_f32_fp8_e32 v[22:23], v75
	v_cvt_pk_f32_fp8_sdwa v[30:31], v75 src0_sel:WORD_1
	v_mul_f32_e32 v231, s37, v18
	v_fmac_f32_e32 v231, s36, v16
	v_fmac_f32_e32 v231, s38, v20
	v_fmac_f32_e32 v231, s39, v22
	v_fmac_f32_e32 v40, v104, v231
	v_mul_f32_e32 v231, s37, v19
	v_fmac_f32_e32 v231, s36, v17
	v_fmac_f32_e32 v231, s38, v21
	v_fmac_f32_e32 v231, s39, v23
	v_fmac_f32_e32 v41, v105, v231
	v_mul_f32_e32 v231, s37, v26
	v_fmac_f32_e32 v231, s36, v24
	v_fmac_f32_e32 v231, s38, v28
	v_fmac_f32_e32 v231, s39, v30
	v_fmac_f32_e32 v42, v106, v231
	v_mul_f32_e32 v231, s37, v27
	v_fmac_f32_e32 v231, s36, v25
	v_fmac_f32_e32 v231, s38, v29
	v_fmac_f32_e32 v231, s39, v31
	v_fmac_f32_e32 v43, v107, v231
	v_mul_f32_e32 v232, v40, v40
	v_fmac_f32_e32 v232, v41, v41
	v_mul_f32_e32 v233, v42, v42
	v_fmac_f32_e32 v233, v43, v43
	v_add_f32_e32 v232, v232, v233
	v_add_f32_e32 v230, v230, v232
	v_cvt_pk_f32_fp8_e32 v[16:17], v76
	v_cvt_pk_f32_fp8_sdwa v[24:25], v76 src0_sel:WORD_1
	v_cvt_pk_f32_fp8_e32 v[18:19], v77
	v_cvt_pk_f32_fp8_sdwa v[26:27], v77 src0_sel:WORD_1
	v_cvt_pk_f32_fp8_e32 v[20:21], v78
	v_cvt_pk_f32_fp8_sdwa v[28:29], v78 src0_sel:WORD_1
	v_cvt_pk_f32_fp8_e32 v[22:23], v79
	v_cvt_pk_f32_fp8_sdwa v[30:31], v79 src0_sel:WORD_1
	v_mul_f32_e32 v231, s37, v18
	v_fmac_f32_e32 v231, s36, v16
	v_fmac_f32_e32 v231, s38, v20
	v_fmac_f32_e32 v231, s39, v22
	v_fmac_f32_e32 v44, v108, v231
	v_mul_f32_e32 v231, s37, v19
	v_fmac_f32_e32 v231, s36, v17
	v_fmac_f32_e32 v231, s38, v21
	v_fmac_f32_e32 v231, s39, v23
	v_fmac_f32_e32 v45, v109, v231
	v_mul_f32_e32 v231, s37, v26
	v_fmac_f32_e32 v231, s36, v24
	v_fmac_f32_e32 v231, s38, v28
	v_fmac_f32_e32 v231, s39, v30
	v_fmac_f32_e32 v46, v110, v231
	v_mul_f32_e32 v231, s37, v27
	v_fmac_f32_e32 v231, s36, v25
	v_fmac_f32_e32 v231, s38, v29
	v_fmac_f32_e32 v231, s39, v31
	v_fmac_f32_e32 v47, v111, v231
	v_mul_f32_e32 v232, v44, v44
	v_fmac_f32_e32 v232, v45, v45
	v_mul_f32_e32 v233, v46, v46
	v_fmac_f32_e32 v233, v47, v47
	v_add_f32_e32 v232, v232, v233
	v_add_f32_e32 v230, v230, v232
	v_cvt_pk_f32_fp8_e32 v[16:17], v80
	v_cvt_pk_f32_fp8_sdwa v[24:25], v80 src0_sel:WORD_1
	v_cvt_pk_f32_fp8_e32 v[18:19], v81
	v_cvt_pk_f32_fp8_sdwa v[26:27], v81 src0_sel:WORD_1
	v_cvt_pk_f32_fp8_e32 v[20:21], v82
	v_cvt_pk_f32_fp8_sdwa v[28:29], v82 src0_sel:WORD_1
	v_cvt_pk_f32_fp8_e32 v[22:23], v83
	v_cvt_pk_f32_fp8_sdwa v[30:31], v83 src0_sel:WORD_1
	v_mul_f32_e32 v231, s37, v18
	v_fmac_f32_e32 v231, s36, v16
	v_fmac_f32_e32 v231, s38, v20
	v_fmac_f32_e32 v231, s39, v22
	v_fmac_f32_e32 v48, v112, v231
	v_mul_f32_e32 v231, s37, v19
	v_fmac_f32_e32 v231, s36, v17
	v_fmac_f32_e32 v231, s38, v21
	v_fmac_f32_e32 v231, s39, v23
	v_fmac_f32_e32 v49, v113, v231
	v_mul_f32_e32 v231, s37, v26
	v_fmac_f32_e32 v231, s36, v24
	v_fmac_f32_e32 v231, s38, v28
	v_fmac_f32_e32 v231, s39, v30
	v_fmac_f32_e32 v50, v114, v231
	v_mul_f32_e32 v231, s37, v27
	v_fmac_f32_e32 v231, s36, v25
	v_fmac_f32_e32 v231, s38, v29
	v_fmac_f32_e32 v231, s39, v31
	v_fmac_f32_e32 v51, v115, v231
	v_mul_f32_e32 v232, v48, v48
	v_fmac_f32_e32 v232, v49, v49
	v_mul_f32_e32 v233, v50, v50
	v_fmac_f32_e32 v233, v51, v51
	v_add_f32_e32 v232, v232, v233
	v_add_f32_e32 v230, v230, v232
	v_cvt_pk_f32_fp8_e32 v[16:17], v84
	v_cvt_pk_f32_fp8_sdwa v[24:25], v84 src0_sel:WORD_1
	v_cvt_pk_f32_fp8_e32 v[18:19], v85
	v_cvt_pk_f32_fp8_sdwa v[26:27], v85 src0_sel:WORD_1
	v_cvt_pk_f32_fp8_e32 v[20:21], v86
	v_cvt_pk_f32_fp8_sdwa v[28:29], v86 src0_sel:WORD_1
	v_cvt_pk_f32_fp8_e32 v[22:23], v87
	v_cvt_pk_f32_fp8_sdwa v[30:31], v87 src0_sel:WORD_1
	v_mul_f32_e32 v231, s37, v18
	v_fmac_f32_e32 v231, s36, v16
	v_fmac_f32_e32 v231, s38, v20
	v_fmac_f32_e32 v231, s39, v22
	v_fmac_f32_e32 v52, v116, v231
	v_mul_f32_e32 v231, s37, v19
	v_fmac_f32_e32 v231, s36, v17
	v_fmac_f32_e32 v231, s38, v21
	v_fmac_f32_e32 v231, s39, v23
	v_fmac_f32_e32 v53, v117, v231
	v_mul_f32_e32 v231, s37, v26
	v_fmac_f32_e32 v231, s36, v24
	v_fmac_f32_e32 v231, s38, v28
	v_fmac_f32_e32 v231, s39, v30
	v_fmac_f32_e32 v54, v118, v231
	v_mul_f32_e32 v231, s37, v27
	v_fmac_f32_e32 v231, s36, v25
	v_fmac_f32_e32 v231, s38, v29
	v_fmac_f32_e32 v231, s39, v31
	v_fmac_f32_e32 v55, v119, v231
	v_mul_f32_e32 v232, v52, v52
	v_fmac_f32_e32 v232, v53, v53
	v_mul_f32_e32 v233, v54, v54
	v_fmac_f32_e32 v233, v55, v55
	v_add_f32_e32 v232, v232, v233
	v_add_f32_e32 v230, v230, v232
	v_cvt_pk_f32_fp8_e32 v[16:17], v88
	v_cvt_pk_f32_fp8_sdwa v[24:25], v88 src0_sel:WORD_1
	v_cvt_pk_f32_fp8_e32 v[18:19], v89
	v_cvt_pk_f32_fp8_sdwa v[26:27], v89 src0_sel:WORD_1
	v_cvt_pk_f32_fp8_e32 v[20:21], v90
	v_cvt_pk_f32_fp8_sdwa v[28:29], v90 src0_sel:WORD_1
	v_cvt_pk_f32_fp8_e32 v[22:23], v91
	v_cvt_pk_f32_fp8_sdwa v[30:31], v91 src0_sel:WORD_1
	v_mul_f32_e32 v231, s37, v18
	v_fmac_f32_e32 v231, s36, v16
	v_fmac_f32_e32 v231, s38, v20
	v_fmac_f32_e32 v231, s39, v22
	v_fmac_f32_e32 v56, v120, v231
	v_mul_f32_e32 v231, s37, v19
	v_fmac_f32_e32 v231, s36, v17
	v_fmac_f32_e32 v231, s38, v21
	v_fmac_f32_e32 v231, s39, v23
	v_fmac_f32_e32 v57, v121, v231
	v_mul_f32_e32 v231, s37, v26
	v_fmac_f32_e32 v231, s36, v24
	v_fmac_f32_e32 v231, s38, v28
	v_fmac_f32_e32 v231, s39, v30
	v_fmac_f32_e32 v58, v122, v231
	v_mul_f32_e32 v231, s37, v27
	v_fmac_f32_e32 v231, s36, v25
	v_fmac_f32_e32 v231, s38, v29
	v_fmac_f32_e32 v231, s39, v31
	v_fmac_f32_e32 v59, v123, v231
	v_mul_f32_e32 v232, v56, v56
	v_fmac_f32_e32 v232, v57, v57
	v_mul_f32_e32 v233, v58, v58
	v_fmac_f32_e32 v233, v59, v59
	v_add_f32_e32 v232, v232, v233
	v_add_f32_e32 v230, v230, v232
	v_cvt_pk_f32_fp8_e32 v[16:17], v92
	v_cvt_pk_f32_fp8_sdwa v[24:25], v92 src0_sel:WORD_1
	v_cvt_pk_f32_fp8_e32 v[18:19], v93
	v_cvt_pk_f32_fp8_sdwa v[26:27], v93 src0_sel:WORD_1
	v_cvt_pk_f32_fp8_e32 v[20:21], v94
	v_cvt_pk_f32_fp8_sdwa v[28:29], v94 src0_sel:WORD_1
	v_cvt_pk_f32_fp8_e32 v[22:23], v95
	v_cvt_pk_f32_fp8_sdwa v[30:31], v95 src0_sel:WORD_1
	v_mul_f32_e32 v231, s37, v18
	v_fmac_f32_e32 v231, s36, v16
	v_fmac_f32_e32 v231, s38, v20
	v_fmac_f32_e32 v231, s39, v22
	v_fmac_f32_e32 v60, v124, v231
	v_mul_f32_e32 v231, s37, v19
	v_fmac_f32_e32 v231, s36, v17
	v_fmac_f32_e32 v231, s38, v21
	v_fmac_f32_e32 v231, s39, v23
	v_fmac_f32_e32 v61, v125, v231
	v_mul_f32_e32 v231, s37, v26
	v_fmac_f32_e32 v231, s36, v24
	v_fmac_f32_e32 v231, s38, v28
	v_fmac_f32_e32 v231, s39, v30
	v_fmac_f32_e32 v62, v126, v231
	v_mul_f32_e32 v231, s37, v27
	v_fmac_f32_e32 v231, s36, v25
	v_fmac_f32_e32 v231, s38, v29
	v_fmac_f32_e32 v231, s39, v31
	v_fmac_f32_e32 v63, v127, v231
	v_mul_f32_e32 v232, v60, v60
	v_fmac_f32_e32 v232, v61, v61
	v_mul_f32_e32 v233, v62, v62
	v_fmac_f32_e32 v233, v63, v63
	v_add_f32_e32 v232, v232, v233
	v_add_f32_e32 v230, v230, v232
	s_cmp_eq_u32 s26, s27
	s_cbranch_scc1 .Lp11_samecoef
	s_lshl_b32 s34, s27, 14
	s_add_u32 s20, s50, 0xa0000
	s_addc_u32 s21, s51, 0
	s_add_u32 s20, s20, s34
	s_addc_u32 s21, s21, 0
	s_add_u32 s44, s18, 0x1000
	s_addc_u32 s45, s19, 0
	s_add_u32 s46, s20, 0x1000
	s_addc_u32 s47, s21, 0
	s_add_u32 s22, s20, 0x2000
	s_addc_u32 s23, s21, 0
	s_add_u32 s48, s20, 0x3000
	s_addc_u32 s49, s21, 0
	global_load_dwordx4 v[128:131], v2, s[18:19] offset:0
	global_load_dwordx4 v[132:135], v2, s[18:19] offset:1024
	global_load_dwordx4 v[136:139], v2, s[18:19] offset:2048
	global_load_dwordx4 v[140:143], v2, s[18:19] offset:3072
	global_load_dwordx4 v[144:147], v2, s[44:45] offset:0
	global_load_dwordx4 v[148:151], v2, s[44:45] offset:1024
	global_load_dwordx4 v[152:155], v2, s[44:45] offset:2048
	global_load_dwordx4 v[156:159], v2, s[44:45] offset:3072
	global_load_dwordx4 v[160:163], v2, s[20:21] offset:0
	global_load_dwordx4 v[164:167], v2, s[20:21] offset:1024
	global_load_dwordx4 v[168:171], v2, s[20:21] offset:2048
	global_load_dwordx4 v[172:175], v2, s[20:21] offset:3072
	global_load_dwordx4 v[176:179], v2, s[46:47] offset:0
	global_load_dwordx4 v[180:183], v2, s[46:47] offset:1024
	global_load_dwordx4 v[184:187], v2, s[46:47] offset:2048
	global_load_dwordx4 v[188:191], v2, s[46:47] offset:3072
	global_load_dwordx4 v[192:195], v2, s[22:23] offset:0
	global_load_dwordx4 v[196:199], v2, s[22:23] offset:1024
	global_load_dwordx4 v[200:203], v2, s[22:23] offset:2048
	global_load_dwordx4 v[204:207], v2, s[22:23] offset:3072
	global_load_dwordx4 v[208:211], v2, s[48:49] offset:0
	global_load_dwordx4 v[212:215], v2, s[48:49] offset:1024
	global_load_dwordx4 v[216:219], v2, s[48:49] offset:2048
	global_load_dwordx4 v[220:223], v2, s[48:49] offset:3072
	s_mov_b32 s26, s27
.Lp11_samecoef:
	ds_bpermute_b32 v232, v224, v230
	s_waitcnt lgkmcnt(0)
	v_add_f32_e32 v230, v230, v232
	ds_bpermute_b32 v232, v225, v230
	s_waitcnt lgkmcnt(0)
	v_add_f32_e32 v230, v230, v232
	ds_bpermute_b32 v232, v226, v230
	s_waitcnt lgkmcnt(0)
	v_add_f32_e32 v230, v230, v232
	ds_bpermute_b32 v232, v227, v230
	s_waitcnt lgkmcnt(0)
	v_add_f32_e32 v230, v230, v232
	ds_bpermute_b32 v232, v228, v230
	s_waitcnt lgkmcnt(0)
	v_add_f32_e32 v230, v230, v232
	ds_bpermute_b32 v232, v229, v230
	s_waitcnt lgkmcnt(0)
	v_add_f32_e32 v230, v230, v232
	v_mov_b32_e32 v232, s42
	v_fmac_f32_e32 v232, s41, v230
	v_rsq_f32_e32 v232, v232
	s_waitcnt vmcnt(0)
	v_mul_f32_e32 v32, v32, v232
	v_mul_f32_e32 v32, v32, v128
	v_add_f32_e32 v231, 1.0, v192
	v_fma_f32 v32, v32, v231, v160
	v_mul_f32_e32 v33, v33, v232
	v_mul_f32_e32 v33, v33, v129
	v_add_f32_e32 v231, 1.0, v193
	v_fma_f32 v33, v33, v231, v161
	v_mul_f32_e32 v34, v34, v232
	v_mul_f32_e32 v34, v34, v130
	v_add_f32_e32 v231, 1.0, v194
	v_fma_f32 v34, v34, v231, v162
	v_mul_f32_e32 v35, v35, v232
	v_mul_f32_e32 v35, v35, v131
	v_add_f32_e32 v231, 1.0, v195
	v_fma_f32 v35, v35, v231, v163
	global_store_dwordx4 v2, v[32:35], s[8:9] offset:0 nt
	v_mul_f32_e32 v36, v36, v232
	v_mul_f32_e32 v36, v36, v132
	v_add_f32_e32 v231, 1.0, v196
	v_fma_f32 v36, v36, v231, v164
	v_mul_f32_e32 v37, v37, v232
	v_mul_f32_e32 v37, v37, v133
	v_add_f32_e32 v231, 1.0, v197
	v_fma_f32 v37, v37, v231, v165
	v_mul_f32_e32 v38, v38, v232
	v_mul_f32_e32 v38, v38, v134
	v_add_f32_e32 v231, 1.0, v198
	v_fma_f32 v38, v38, v231, v166
	v_mul_f32_e32 v39, v39, v232
	v_mul_f32_e32 v39, v39, v135
	v_add_f32_e32 v231, 1.0, v199
	v_fma_f32 v39, v39, v231, v167
	global_store_dwordx4 v2, v[36:39], s[8:9] offset:1024 nt
	v_mul_f32_e32 v40, v40, v232
	v_mul_f32_e32 v40, v40, v136
	v_add_f32_e32 v231, 1.0, v200
	v_fma_f32 v40, v40, v231, v168
	v_mul_f32_e32 v41, v41, v232
	v_mul_f32_e32 v41, v41, v137
	v_add_f32_e32 v231, 1.0, v201
	v_fma_f32 v41, v41, v231, v169
	v_mul_f32_e32 v42, v42, v232
	v_mul_f32_e32 v42, v42, v138
	v_add_f32_e32 v231, 1.0, v202
	v_fma_f32 v42, v42, v231, v170
	v_mul_f32_e32 v43, v43, v232
	v_mul_f32_e32 v43, v43, v139
	v_add_f32_e32 v231, 1.0, v203
	v_fma_f32 v43, v43, v231, v171
	global_store_dwordx4 v2, v[40:43], s[8:9] offset:2048 nt
	v_mul_f32_e32 v44, v44, v232
	v_mul_f32_e32 v44, v44, v140
	v_add_f32_e32 v231, 1.0, v204
	v_fma_f32 v44, v44, v231, v172
	v_mul_f32_e32 v45, v45, v232
	v_mul_f32_e32 v45, v45, v141
	v_add_f32_e32 v231, 1.0, v205
	v_fma_f32 v45, v45, v231, v173
	v_mul_f32_e32 v46, v46, v232
	v_mul_f32_e32 v46, v46, v142
	v_add_f32_e32 v231, 1.0, v206
	v_fma_f32 v46, v46, v231, v174
	v_mul_f32_e32 v47, v47, v232
	v_mul_f32_e32 v47, v47, v143
	v_add_f32_e32 v231, 1.0, v207
	v_fma_f32 v47, v47, v231, v175
	global_store_dwordx4 v2, v[44:47], s[8:9] offset:3072 nt
	v_mul_f32_e32 v48, v48, v232
	v_mul_f32_e32 v48, v48, v144
	v_add_f32_e32 v231, 1.0, v208
	v_fma_f32 v48, v48, v231, v176
	v_mul_f32_e32 v49, v49, v232
	v_mul_f32_e32 v49, v49, v145
	v_add_f32_e32 v231, 1.0, v209
	v_fma_f32 v49, v49, v231, v177
	v_mul_f32_e32 v50, v50, v232
	v_mul_f32_e32 v50, v50, v146
	v_add_f32_e32 v231, 1.0, v210
	v_fma_f32 v50, v50, v231, v178
	v_mul_f32_e32 v51, v51, v232
	v_mul_f32_e32 v51, v51, v147
	v_add_f32_e32 v231, 1.0, v211
	v_fma_f32 v51, v51, v231, v179
	global_store_dwordx4 v2, v[48:51], s[32:33] offset:0 nt
	v_mul_f32_e32 v52, v52, v232
	v_mul_f32_e32 v52, v52, v148
	v_add_f32_e32 v231, 1.0, v212
	v_fma_f32 v52, v52, v231, v180
	v_mul_f32_e32 v53, v53, v232
	v_mul_f32_e32 v53, v53, v149
	v_add_f32_e32 v231, 1.0, v213
	v_fma_f32 v53, v53, v231, v181
	v_mul_f32_e32 v54, v54, v232
	v_mul_f32_e32 v54, v54, v150
	v_add_f32_e32 v231, 1.0, v214
	v_fma_f32 v54, v54, v231, v182
	v_mul_f32_e32 v55, v55, v232
	v_mul_f32_e32 v55, v55, v151
	v_add_f32_e32 v231, 1.0, v215
	v_fma_f32 v55, v55, v231, v183
	global_store_dwordx4 v2, v[52:55], s[32:33] offset:1024 nt
	v_mul_f32_e32 v56, v56, v232
	v_mul_f32_e32 v56, v56, v152
	v_add_f32_e32 v231, 1.0, v216
	v_fma_f32 v56, v56, v231, v184
	v_mul_f32_e32 v57, v57, v232
	v_mul_f32_e32 v57, v57, v153
	v_add_f32_e32 v231, 1.0, v217
	v_fma_f32 v57, v57, v231, v185
	v_mul_f32_e32 v58, v58, v232
	v_mul_f32_e32 v58, v58, v154
	v_add_f32_e32 v231, 1.0, v218
	v_fma_f32 v58, v58, v231, v186
	v_mul_f32_e32 v59, v59, v232
	v_mul_f32_e32 v59, v59, v155
	v_add_f32_e32 v231, 1.0, v219
	v_fma_f32 v59, v59, v231, v187
	global_store_dwordx4 v2, v[56:59], s[32:33] offset:2048 nt
	v_mul_f32_e32 v60, v60, v232
	v_mul_f32_e32 v60, v60, v156
	v_add_f32_e32 v231, 1.0, v220
	v_fma_f32 v60, v60, v231, v188
	v_mul_f32_e32 v61, v61, v232
	v_mul_f32_e32 v61, v61, v157
	v_add_f32_e32 v231, 1.0, v221
	v_fma_f32 v61, v61, v231, v189
	v_mul_f32_e32 v62, v62, v232
	v_mul_f32_e32 v62, v62, v158
	v_add_f32_e32 v231, 1.0, v222
	v_fma_f32 v62, v62, v231, v190
	v_mul_f32_e32 v63, v63, v232
	v_mul_f32_e32 v63, v63, v159
	v_add_f32_e32 v231, 1.0, v223
	v_fma_f32 v63, v63, v231, v191
	global_store_dwordx4 v2, v[60:63], s[32:33] offset:3072 nt
	s_add_i32 s2, s2, s4
	s_cmpk_lt_i32 s2, 0x2000
	s_cbranch_scc1 .Lp11_row
